# mLSTM item prologues: all four gate values of a token pair fetched in a single round trip (second pair's address formed early in scratch registers)
# speedup vs baseline: 1.0057x; 1.0012x over previous
; DI float softcap(float x) { return 15.0f * tanhf(x * (1.0f / 15.0f)); }
; DI float logsigmoid(float y) { return fminf(y, 0.f) - log1pf(__expf(-fabsf(y))); }
; DI void mlstm_pass1(const Params& P, LAS unsigned char* lds, int st, int g) {
;     ...
;     if (wid < nchunks) { const int t0c = chunk_tok0(wid);
;         const int p0 = dir ? 127 - 2 * lane : 2 * lane, p1 = dir ? 126 - 2 * lane : 2 * lane + 1;
;         const float* g0 = gates + (size_t)(t0c + p0) * 16; const float* g1 = gates + (size_t)(t0c + p1) * 16;
;         const float li0 = softcap(g0[dir * 8 + h]), li1 = softcap(g1[dir * 8 + h]); const float lf0 = logsigmoid(softcap(g0[dir * 8 + 4 + h])), lf1 = logsigmoid(softcap(g1[dir * 8 + 4 + h]));
.LBB0_445:
	v_and_b32_e32 v5, 63, v4
	v_lshlrev_b32_e32 v2, 1, v5
	s_lshl_b32 s2, s5, 7
	v_xor_b32_e32 v0, 0x7f, v2
	s_add_i32 s6, s4, s2
	v_cndmask_b32_e64 v6, v0, v2, s[0:1]
	v_add_u32_e32 v0, s6, v6
	v_ashrrev_i32_e32 v1, 31, v0
	v_lshlrev_b64 v[0:1], 6, v[0:1]
	s_and_b32 s2, s38, -5
	v_lshl_add_u64 v[0:1], s[22:23], 0, v[0:1]
	s_ashr_i32 s3, s2, 31
	v_lshl_add_u64 v[0:1], s[2:3], 2, v[0:1]
	v_sub_u32_e32 v16, 0x7e, v2
	v_or_b32_e32 v17, 1, v2
	v_cndmask_b32_e64 v16, v16, v17, s[0:1]
	v_add_u32_e32 v16, s6, v16
	v_ashrrev_i32_e32 v17, 31, v16
	v_lshlrev_b64 v[16:17], 6, v[16:17]
	v_lshl_add_u64 v[16:17], s[22:23], 0, v[16:17]
	v_lshl_add_u64 v[16:17], s[2:3], 2, v[16:17]
	global_load_dword v3, v[0:1], off
	global_load_dword v15, v[0:1], off offset:16
	global_load_dword v18, v[16:17], off
	global_load_dword v19, v[16:17], off offset:16
	s_waitcnt vmcnt(0)
	v_mul_f32_e32 v7, 0x3d888889, v3
	v_cmp_nlt_f32_e64 s[4:5], |v7|, s49
	s_and_saveexec_b64 s[8:9], s[4:5]
	s_xor_b64 s[4:5], exec, s[8:9]
	s_cbranch_execz .LBB0_447
	v_add_f32_e64 v3, |v7|, |v7|
	v_mul_f32_e32 v8, 0x3fb8aa3b, v3
	v_rndne_f32_e32 v9, v8
	v_sub_f32_e32 v10, v8, v9
	v_fma_f32 v8, v3, s50, -v8
	v_fmac_f32_e32 v8, 0x32a5705f, v3
	v_add_f32_e32 v8, v10, v8
	v_cvt_i32_f32_e32 v9, v9
	v_exp_f32_e32 v8, v8
	v_cmp_ngt_f32_e32 vcc, s51, v3
	v_ldexp_f32 v8, v8, v9
	s_nop 0
	v_cndmask_b32_e32 v8, 0, v8, vcc
	v_cmp_nlt_f32_e32 vcc, s52, v3
	s_nop 1
	v_cndmask_b32_e32 v3, v149, v8, vcc
	v_add_f32_e32 v3, 1.0, v3
	v_rcp_f32_e32 v3, v3
	s_nop 0
	v_fma_f32 v9, v3, -2.0, 1.0
.LBB0_447:
	s_andn2_saveexec_b64 s[4:5], s[4:5]
	v_mul_f32_e32 v3, v7, v7
	v_fmamk_f32 v8, v3, 0xbbbac73d, v147
	v_fmaak_f32 v8, v3, v8, 0xbd5c1c4e
	v_fmaak_f32 v8, v3, v8, 0x3e088382
	v_fmaak_f32 v8, v3, v8, 0xbeaaaa99
	v_mul_f32_e64 v8, |v7|, v8
	v_fma_f32 v9, v3, v8, |v7|
	s_or_b64 exec, exec, s[4:5]
	v_sub_u32_e32 v3, 0x7e, v2
	v_or_b32_e32 v2, 1, v2
	v_cndmask_b32_e64 v8, v3, v2, s[0:1]
	v_add_u32_e32 v2, s6, v8
	v_ashrrev_i32_e32 v3, 31, v2
	v_lshlrev_b64 v[2:3], 6, v[2:3]
	v_lshl_add_u64 v[2:3], s[22:23], 0, v[2:3]
	v_lshl_add_u64 v[2:3], s[2:3], 2, v[2:3]
	v_mov_b32_e32 v10, v18
	s_waitcnt vmcnt(0)
	v_mul_f32_e32 v10, 0x3d888889, v10
	v_cmp_nlt_f32_e64 s[0:1], |v10|, s49
	s_and_saveexec_b64 s[2:3], s[0:1]
	s_xor_b64 s[0:1], exec, s[2:3]
	s_cbranch_execz .LBB0_451
	v_add_f32_e64 v11, |v10|, |v10|
	v_mul_f32_e32 v12, 0x3fb8aa3b, v11
	v_rndne_f32_e32 v13, v12
	v_sub_f32_e32 v14, v12, v13
	v_fma_f32 v12, v11, s50, -v12
	v_fmac_f32_e32 v12, 0x32a5705f, v11
	v_add_f32_e32 v12, v14, v12
	v_cvt_i32_f32_e32 v13, v13
	v_exp_f32_e32 v12, v12
	v_cmp_ngt_f32_e32 vcc, s51, v11
	v_ldexp_f32 v12, v12, v13
	s_nop 0
	v_cndmask_b32_e32 v12, 0, v12, vcc
	v_cmp_nlt_f32_e32 vcc, s52, v11
	s_nop 1
	v_cndmask_b32_e32 v11, v149, v12, vcc
	v_add_f32_e32 v11, 1.0, v11
	v_rcp_f32_e32 v11, v11
	s_nop 0
	v_fma_f32 v11, v11, -2.0, 1.0

; DI float softcap(float x) { return 15.0f * tanhf(x * (1.0f / 15.0f)); }
; DI float logsigmoid(float y) { return fminf(y, 0.f) - log1pf(__expf(-fabsf(y))); }
; DI void mlstm_pass1(const Params& P, LAS unsigned char* lds, int st, int g) {
;     ...
;         const int p0 = dir ? 127 - 2 * lane : 2 * lane, p1 = dir ? 126 - 2 * lane : 2 * lane + 1;
;         const float* g0 = gates + (size_t)(t0c + p0) * 16; const float* g1 = gates + (size_t)(t0c + p1) * 16;
;         const float li0 = softcap(g0[dir * 8 + h]), li1 = softcap(g1[dir * 8 + h]); const float lf0 = logsigmoid(softcap(g0[dir * 8 + 4 + h])), lf1 = logsigmoid(softcap(g1[dir * 8 + 4 + h]));
.LBB0_455:
	s_andn2_saveexec_b64 s[0:1], s[0:1]
	v_mul_f32_e32 v0, v12, v12
	v_fmamk_f32 v1, v0, 0xbbbac73d, v147
	v_fmaak_f32 v1, v0, v1, 0xbd5c1c4e
	v_fmaak_f32 v1, v0, v1, 0x3e088382
	v_fmaak_f32 v1, v0, v1, 0xbeaaaa99
	v_mul_f32_e64 v1, |v12|, v1
	v_fma_f32 v13, v0, v1, |v12|
	s_or_b64 exec, exec, s[0:1]
	v_mov_b32_e32 v0, v19
	s_waitcnt vmcnt(0)
	v_mul_f32_e32 v0, 0x3d888889, v0
	v_cmp_nlt_f32_e64 s[0:1], |v0|, s49
	s_and_saveexec_b64 s[2:3], s[0:1]
	s_xor_b64 s[0:1], exec, s[2:3]
	s_cbranch_execz .LBB0_459
	v_add_f32_e64 v1, |v0|, |v0|
	v_mul_f32_e32 v2, 0x3fb8aa3b, v1
	v_rndne_f32_e32 v3, v2
	v_sub_f32_e32 v14, v2, v3
	v_fma_f32 v2, v1, s50, -v2
	v_fmac_f32_e32 v2, 0x32a5705f, v1
	v_add_f32_e32 v2, v14, v2
	v_cvt_i32_f32_e32 v3, v3
	v_exp_f32_e32 v2, v2
	v_cmp_ngt_f32_e32 vcc, s51, v1
	v_ldexp_f32 v2, v2, v3
	s_nop 0
	v_cndmask_b32_e32 v2, 0, v2, vcc
	v_cmp_nlt_f32_e32 vcc, s52, v1
	s_nop 1
	v_cndmask_b32_e32 v1, v149, v2, vcc
	v_add_f32_e32 v1, 1.0, v1
	v_rcp_f32_e32 v1, v1
	s_nop 0
	v_fma_f32 v1, v1, -2.0, 1.0

; DI float softcap(float x) { return 15.0f * tanhf(x * (1.0f / 15.0f)); }
; DI float logsigmoid(float y) { return fminf(y, 0.f) - log1pf(__expf(-fabsf(y))); }
; template <bool PASS2, int DIRT>
; DI void mlstm_item(const Params& P, LAS unsigned char* lds, int st, int g) {
;     ...
;     if (wid < nchunks) { const int t0c = chunk_tok0(wid);
;         const int p0 = dir ? 127 - 2 * lane : 2 * lane, p1 = dir ? 126 - 2 * lane : 2 * lane + 1;
;         const float* g0 = gates + (size_t)(t0c + p0) * 16; const float* g1 = gates + (size_t)(t0c + p1) * 16;
;         const float li0 = softcap(g0[dir * 8 + h]), li1 = softcap(g1[dir * 8 + h]); const float lf0 = logsigmoid(softcap(g0[dir * 8 + 4 + h])), lf1 = logsigmoid(softcap(g1[dir * 8 + 4 + h]));
.LBB0_714:
	s_or_b64 exec, exec, s[2:3]
	s_bfe_u32 s0, s4, 0x10002
	s_and_b32 s48, s4, 3
	s_cmp_gt_i32 s1, 7
	s_cbranch_scc1 .LBB0_734
	s_lshl_b32 s2, s0, 14
	s_lshl_b32 s3, s96, 10
	s_lshl_b32 s4, s1, 7
	v_and_b32_e32 v65, 63, v70
	s_or_b32 s2, s2, 0x3f80
	s_add_i32 s3, s3, s4
	s_sub_i32 s6, s2, s3
	v_lshlrev_b32_e32 v71, 1, v65
	v_bitop3_b32 v66, v71, s6, v200 bitop3:0xde
	v_ashrrev_i32_e32 v67, 31, v66
	v_lshlrev_b64 v[66:67], 6, v[66:67]
	v_lshl_add_u64 v[66:67], s[38:39], 0, v[66:67]
	s_lshl_b32 s40, s48, 2
	v_lshl_add_u64 v[66:67], v[66:67], 0, s[40:41]
	v_sub_u32_e32 v246, s6, v71
	v_add_u32_e32 v246, 0x7e, v246
	v_ashrrev_i32_e32 v247, 31, v246
	v_lshlrev_b64 v[246:247], 6, v[246:247]
	v_lshl_add_u64 v[246:247], s[38:39], 0, v[246:247]
	v_lshl_add_u64 v[246:247], v[246:247], 0, s[40:41]
	global_load_dword v68, v[66:67], off offset:32
	global_load_dword v244, v[66:67], off offset:48
	global_load_dword v248, v[246:247], off offset:32
	global_load_dword v245, v[246:247], off offset:48
	s_waitcnt vmcnt(0)
	v_mul_f32_e32 v72, 0x3d888889, v68
	v_cmp_nlt_f32_e64 s[2:3], |v72|, s66
	s_and_saveexec_b64 s[4:5], s[2:3]
	s_xor_b64 s[2:3], exec, s[4:5]
	s_cbranch_execz .LBB0_717
	v_add_f32_e64 v68, |v72|, |v72|
	v_mul_f32_e32 v69, 0x3fb8aa3b, v68
	v_rndne_f32_e32 v73, v69
	s_mov_b32 s4, 0x3fb8aa3b
	v_sub_f32_e32 v74, v69, v73
	v_fma_f32 v69, v68, s4, -v69
	v_fmac_f32_e32 v69, 0x32a5705f, v68
	v_add_f32_e32 v69, v74, v69
	v_cvt_i32_f32_e32 v73, v73
	v_exp_f32_e32 v69, v69
	v_cmp_ngt_f32_e64 s[4:5], s68, v68
	v_ldexp_f32 v69, v69, v73
	s_nop 0
	v_cndmask_b32_e64 v69, 0, v69, s[4:5]
	v_cmp_nlt_f32_e64 s[4:5], s69, v68
	s_nop 1
	v_cndmask_b32_e64 v68, v201, v69, s[4:5]
	v_add_f32_e32 v68, 1.0, v68
	v_rcp_f32_e32 v68, v68
	s_nop 0
	v_fma_f32 v73, v68, -2.0, 1.0
.LBB0_717:
	s_andn2_saveexec_b64 s[2:3], s[2:3]
	v_mul_f32_e32 v68, v72, v72
	v_fmamk_f32 v69, v68, 0xbbbac73d, v198
	v_fmaak_f32 v69, v68, v69, 0xbd5c1c4e
	v_fmaak_f32 v69, v68, v69, 0x3e088382
	v_fmaak_f32 v69, v68, v69, 0xbeaaaa99
	v_mul_f32_e64 v69, |v72|, v69
	v_fma_f32 v73, v68, v69, |v72|
	s_or_b64 exec, exec, s[2:3]
	v_sub_u32_e32 v68, s6, v71
	v_add_u32_e32 v68, 0x7e, v68
	v_ashrrev_i32_e32 v69, 31, v68
	v_lshlrev_b64 v[68:69], 6, v[68:69]
	v_lshl_add_u64 v[68:69], s[38:39], 0, v[68:69]
	v_lshl_add_u64 v[68:69], v[68:69], 0, s[40:41]
	v_mov_b32_e32 v74, v248
	s_waitcnt vmcnt(0)
	v_mul_f32_e32 v74, 0x3d888889, v74
	v_cmp_nlt_f32_e64 s[2:3], |v74|, s66
	s_and_saveexec_b64 s[4:5], s[2:3]
	s_xor_b64 s[2:3], exec, s[4:5]
	s_cbranch_execz .LBB0_721
	v_add_f32_e64 v75, |v74|, |v74|
	v_mul_f32_e32 v76, 0x3fb8aa3b, v75
	v_rndne_f32_e32 v77, v76
	s_mov_b32 s4, 0x3fb8aa3b
	v_sub_f32_e32 v78, v76, v77
	v_fma_f32 v76, v75, s4, -v76
	v_fmac_f32_e32 v76, 0x32a5705f, v75
	v_add_f32_e32 v76, v78, v76
	v_cvt_i32_f32_e32 v77, v77
	v_exp_f32_e32 v76, v76
	v_cmp_ngt_f32_e64 s[4:5], s68, v75
	v_ldexp_f32 v76, v76, v77
	s_nop 0
	v_cndmask_b32_e64 v76, 0, v76, s[4:5]
	v_cmp_nlt_f32_e64 s[4:5], s69, v75
	s_nop 1
	v_cndmask_b32_e64 v75, v201, v76, s[4:5]
	v_add_f32_e32 v75, 1.0, v75
	v_rcp_f32_e32 v75, v75
	s_nop 0
	v_fma_f32 v75, v75, -2.0, 1.0

; DI float softcap(float x) { return 15.0f * tanhf(x * (1.0f / 15.0f)); }
; DI float logsigmoid(float y) { return fminf(y, 0.f) - log1pf(__expf(-fabsf(y))); }
; template <bool PASS2, int DIRT>
; DI void mlstm_item(const Params& P, LAS unsigned char* lds, int st, int g) {
;     ...
;     if (wid < nchunks) { const int t0c = chunk_tok0(wid);
;         const int p0 = dir ? 127 - 2 * lane : 2 * lane, p1 = dir ? 126 - 2 * lane : 2 * lane + 1;
;         const float* g0 = gates + (size_t)(t0c + p0) * 16; const float* g1 = gates + (size_t)(t0c + p1) * 16;
;         const float li0 = softcap(g0[dir * 8 + h]), li1 = softcap(g1[dir * 8 + h]); const float lf0 = logsigmoid(softcap(g0[dir * 8 + 4 + h])), lf1 = logsigmoid(softcap(g1[dir * 8 + 4 + h]));
.LBB0_771:
	s_or_b64 exec, exec, s[2:3]
	s_lshr_b32 s1, s42, 6
	s_bfe_u32 s48, s42, 0x20004
	s_cmp_gt_i32 s0, 7
	s_cbranch_scc1 .LBB0_791
	s_lshl_b32 s2, s1, 14
	s_lshl_b32 s3, s96, 10
	v_and_b32_e32 v65, 63, v70
	s_lshl_b32 s4, s0, 7
	s_or_b32 s2, s2, s3
	s_add_i32 s2, s2, s4
	v_lshlrev_b32_e32 v71, 1, v65
	v_or_b32_e32 v68, s2, v71
	v_ashrrev_i32_e32 v69, 31, v68
	v_lshlrev_b64 v[66:67], 6, v[68:69]
	v_lshl_add_u64 v[66:67], s[38:39], 0, v[66:67]
	s_lshl_b32 s40, s48, 2
	v_lshl_add_u64 v[72:73], v[66:67], 0, s[40:41]
	v_or_b32_e32 v246, 1, v68
	v_ashrrev_i32_e32 v247, 31, v246
	v_lshlrev_b64 v[246:247], 6, v[246:247]
	v_lshl_add_u64 v[246:247], s[38:39], 0, v[246:247]
	v_lshl_add_u64 v[246:247], v[246:247], 0, s[40:41]
	global_load_dword v69, v[72:73], off
	global_load_dword v244, v[72:73], off offset:16
	global_load_dword v248, v[246:247], off
	global_load_dword v245, v[246:247], off offset:16
	s_waitcnt vmcnt(0)
	v_mul_f32_e32 v72, 0x3d888889, v69
	v_cmp_nlt_f32_e64 s[2:3], |v72|, s66
	s_and_saveexec_b64 s[4:5], s[2:3]
	s_xor_b64 s[2:3], exec, s[4:5]
	s_cbranch_execz .LBB0_774
	v_add_f32_e64 v69, |v72|, |v72|
	v_mul_f32_e32 v73, 0x3fb8aa3b, v69
	v_rndne_f32_e32 v74, v73
	s_mov_b32 s4, 0x3fb8aa3b
	v_sub_f32_e32 v75, v73, v74
	v_fma_f32 v73, v69, s4, -v73
	v_fmac_f32_e32 v73, 0x32a5705f, v69
	v_add_f32_e32 v73, v75, v73
	v_cvt_i32_f32_e32 v74, v74
	v_exp_f32_e32 v73, v73
	v_cmp_ngt_f32_e64 s[4:5], s68, v69
	v_ldexp_f32 v73, v73, v74
	s_nop 0
	v_cndmask_b32_e64 v73, 0, v73, s[4:5]
	v_cmp_nlt_f32_e64 s[4:5], s69, v69
	s_nop 1
	v_cndmask_b32_e64 v69, v201, v73, s[4:5]
	v_add_f32_e32 v69, 1.0, v69
	v_rcp_f32_e32 v69, v69
	s_nop 0
	v_fma_f32 v73, v69, -2.0, 1.0
.LBB0_774:
	s_andn2_saveexec_b64 s[2:3], s[2:3]
	v_mul_f32_e32 v69, v72, v72
	v_fmamk_f32 v73, v69, 0xbbbac73d, v198
	v_fmaak_f32 v73, v69, v73, 0xbd5c1c4e
	v_fmaak_f32 v73, v69, v73, 0x3e088382
	v_fmaak_f32 v73, v69, v73, 0xbeaaaa99
	v_mul_f32_e64 v73, |v72|, v73
	v_fma_f32 v73, v69, v73, |v72|
	s_or_b64 exec, exec, s[2:3]
	v_or_b32_e32 v68, 1, v68
	v_ashrrev_i32_e32 v69, 31, v68
	v_lshlrev_b64 v[68:69], 6, v[68:69]
	v_lshl_add_u64 v[68:69], s[38:39], 0, v[68:69]
	v_lshl_add_u64 v[74:75], v[68:69], 0, s[40:41]
	v_mov_b32_e32 v74, v248
	s_waitcnt vmcnt(0)
	v_mul_f32_e32 v74, 0x3d888889, v74
	v_cmp_nlt_f32_e64 s[2:3], |v74|, s66
	s_and_saveexec_b64 s[4:5], s[2:3]
	s_xor_b64 s[2:3], exec, s[4:5]
	s_cbranch_execz .LBB0_778
	v_add_f32_e64 v75, |v74|, |v74|
	v_mul_f32_e32 v76, 0x3fb8aa3b, v75
	v_rndne_f32_e32 v77, v76
	s_mov_b32 s4, 0x3fb8aa3b
	v_sub_f32_e32 v78, v76, v77
	v_fma_f32 v76, v75, s4, -v76
	v_fmac_f32_e32 v76, 0x32a5705f, v75
	v_add_f32_e32 v76, v78, v76
	v_cvt_i32_f32_e32 v77, v77
	v_exp_f32_e32 v76, v76
	v_cmp_ngt_f32_e64 s[4:5], s68, v75
	v_ldexp_f32 v76, v76, v77
	s_nop 0
	v_cndmask_b32_e64 v76, 0, v76, s[4:5]
	v_cmp_nlt_f32_e64 s[4:5], s69, v75
	s_nop 1
	v_cndmask_b32_e64 v75, v201, v76, s[4:5]
	v_add_f32_e32 v75, 1.0, v75
	v_rcp_f32_e32 v75, v75
	s_nop 0
	v_fma_f32 v75, v75, -2.0, 1.0
